# conversion wave of the lora/conv phase: its 93 flat_load_dword replaced by global_load_dword (still nt), so the loads no longer pass through the LDS path / lgkmcnt
# speedup vs baseline: 1.0020x; 1.0020x over previous
.LBB0_535:
	s_cmp_lg_u32 s5, 2
	s_cselect_b32 s10, s6, 0x800
	s_cmp_eq_u32 s5, 1
	s_cselect_b32 s7, s16, s18
	s_cselect_b32 s11, s17, s19
	s_cmp_eq_u32 s5, 0
	s_cselect_b32 s5, s15, s11
	s_cselect_b32 s11, s14, s7
	s_mul_hi_i32 s7, s9, s6
	s_mul_i32 s6, s9, s6
	s_lshl_b64 s[6:7], s[6:7], 13
	s_add_u32 s6, s11, s6
	v_and_or_b32 v1, v137, 32, s8
	s_addc_u32 s7, s5, s7
	v_mad_i64_i32 v[4:5], s[8:9], s10, v1, 0
	v_lshl_add_u64 v[4:5], v[4:5], 2, s[6:7]
	s_ashr_i32 s5, s4, 31
	v_and_b32_e32 v1, 31, v137
	v_lshl_add_u64 v[4:5], s[4:5], 2, v[4:5]
	v_lshlrev_b32_e32 v6, 2, v1
	v_mov_b32_e32 v7, v3
	v_lshl_add_u64 v[4:5], v[4:5], 0, v[6:7]
	s_lshl_b32 s92, s10, 2
	v_lshl_add_u64 v[6:7], v[4:5], 0, s[92:93]
	global_load_dword v1, v[4:5], off nt
	global_load_dword v5, v[6:7], off nt
	v_lshl_add_u64 v[8:9], v[6:7], 0, s[92:93]
	global_load_dword v7, v[8:9], off nt
	v_lshl_add_u64 v[10:11], v[8:9], 0, s[92:93]
	global_load_dword v8, v[10:11], off nt
	v_lshl_add_u64 v[10:11], v[10:11], 0, s[92:93]
	global_load_dword v9, v[10:11], off nt
	v_lshl_add_u64 v[12:13], v[10:11], 0, s[92:93]
	global_load_dword v10, v[12:13], off nt
	v_lshl_add_u64 v[12:13], v[12:13], 0, s[92:93]
	global_load_dword v11, v[12:13], off nt
	v_lshl_add_u64 v[14:15], v[12:13], 0, s[92:93]
	global_load_dword v12, v[14:15], off nt
	v_lshl_add_u64 v[14:15], v[14:15], 0, s[92:93]
	global_load_dword v13, v[14:15], off nt
	v_lshl_add_u64 v[16:17], v[14:15], 0, s[92:93]
	global_load_dword v14, v[16:17], off nt
	v_lshl_add_u64 v[16:17], v[16:17], 0, s[92:93]
	global_load_dword v15, v[16:17], off nt
	v_lshl_add_u64 v[18:19], v[16:17], 0, s[92:93]
	global_load_dword v16, v[18:19], off nt
	v_lshl_add_u64 v[18:19], v[18:19], 0, s[92:93]
	global_load_dword v17, v[18:19], off nt
	v_lshl_add_u64 v[20:21], v[18:19], 0, s[92:93]
	global_load_dword v18, v[20:21], off nt
	v_lshl_add_u64 v[20:21], v[20:21], 0, s[92:93]
	global_load_dword v19, v[20:21], off nt
	v_lshl_add_u64 v[22:23], v[20:21], 0, s[92:93]
	global_load_dword v20, v[22:23], off nt
	v_lshl_add_u64 v[22:23], v[22:23], 0, s[92:93]
	global_load_dword v21, v[22:23], off nt
	v_lshl_add_u64 v[24:25], v[22:23], 0, s[92:93]
	global_load_dword v22, v[24:25], off nt
	v_lshl_add_u64 v[24:25], v[24:25], 0, s[92:93]
	global_load_dword v23, v[24:25], off nt
	v_lshl_add_u64 v[26:27], v[24:25], 0, s[92:93]
	global_load_dword v24, v[26:27], off nt
	v_lshl_add_u64 v[26:27], v[26:27], 0, s[92:93]
	global_load_dword v25, v[26:27], off nt
	v_lshl_add_u64 v[28:29], v[26:27], 0, s[92:93]
	global_load_dword v26, v[28:29], off nt
	v_lshl_add_u64 v[28:29], v[28:29], 0, s[92:93]
	global_load_dword v27, v[28:29], off nt
	v_lshl_add_u64 v[30:31], v[28:29], 0, s[92:93]
	global_load_dword v28, v[30:31], off nt
	v_lshl_add_u64 v[30:31], v[30:31], 0, s[92:93]
	global_load_dword v29, v[30:31], off nt
	v_lshl_add_u64 v[32:33], v[30:31], 0, s[92:93]
	global_load_dword v30, v[32:33], off nt
	v_lshl_add_u64 v[32:33], v[32:33], 0, s[92:93]
	global_load_dword v31, v[32:33], off nt
	v_lshl_add_u64 v[34:35], v[32:33], 0, s[92:93]
	global_load_dword v32, v[34:35], off nt
	v_lshl_add_u64 v[34:35], v[34:35], 0, s[92:93]
	global_load_dword v33, v[34:35], off nt
	v_lshl_add_u64 v[36:37], v[34:35], 0, s[92:93]
	global_load_dword v34, v[36:37], off nt
	v_lshl_add_u64 v[36:37], v[36:37], 0, s[92:93]
	global_load_dword v35, v[36:37], off nt
	v_lshl_add_u64 v[38:39], v[36:37], 0, s[92:93]
	global_load_dword v36, v[38:39], off nt
	v_lshl_add_u64 v[38:39], v[38:39], 0, s[92:93]

.LBB0_554:
	s_cmp_lg_u32 s7, 2
	s_cselect_b32 s34, s8, 0x800
	s_cmp_eq_u32 s7, 1
	s_cselect_b32 s9, s16, s18
	s_cselect_b32 s35, s17, s19
	s_cmp_eq_u32 s7, 0
	s_cselect_b32 s7, s15, s35
	s_cselect_b32 s35, s14, s9
	s_mul_hi_i32 s9, s11, s8
	s_mul_i32 s8, s11, s8
	s_lshl_b64 s[8:9], s[8:9], 13
	s_add_u32 s8, s35, s8
	v_or_b32_e32 v37, s10, v4
	s_addc_u32 s9, s7, s9
	v_mad_i64_i32 v[38:39], s[10:11], s34, v37, 0
	v_lshl_add_u64 v[38:39], v[38:39], 2, s[8:9]
	s_ashr_i32 s7, s6, 31
	v_lshl_add_u64 v[38:39], s[6:7], 2, v[38:39]
	v_lshlrev_b32_e32 v40, 2, v6
	v_mov_b32_e32 v41, v3
	v_lshl_add_u64 v[38:39], v[38:39], 0, v[40:41]
	s_lshl_b32 s92, s34, 2
	v_lshl_add_u64 v[40:41], v[38:39], 0, s[92:93]
	global_load_dword v37, v[38:39], off nt
	global_load_dword v38, v[40:41], off nt
	v_lshl_add_u64 v[40:41], v[40:41], 0, s[92:93]
	global_load_dword v39, v[40:41], off nt
	v_lshl_add_u64 v[42:43], v[40:41], 0, s[92:93]
	global_load_dword v40, v[42:43], off nt
	v_lshl_add_u64 v[42:43], v[42:43], 0, s[92:93]
	global_load_dword v41, v[42:43], off nt
	v_lshl_add_u64 v[44:45], v[42:43], 0, s[92:93]
	global_load_dword v42, v[44:45], off nt
	v_lshl_add_u64 v[44:45], v[44:45], 0, s[92:93]
	global_load_dword v43, v[44:45], off nt
	v_lshl_add_u64 v[46:47], v[44:45], 0, s[92:93]
	global_load_dword v44, v[46:47], off nt
	v_lshl_add_u64 v[46:47], v[46:47], 0, s[92:93]
	global_load_dword v45, v[46:47], off nt
	v_lshl_add_u64 v[48:49], v[46:47], 0, s[92:93]
	global_load_dword v46, v[48:49], off nt
	v_lshl_add_u64 v[48:49], v[48:49], 0, s[92:93]
	global_load_dword v47, v[48:49], off nt
	v_lshl_add_u64 v[50:51], v[48:49], 0, s[92:93]
	global_load_dword v48, v[50:51], off nt
	v_lshl_add_u64 v[50:51], v[50:51], 0, s[92:93]
	global_load_dword v49, v[50:51], off nt
	v_lshl_add_u64 v[52:53], v[50:51], 0, s[92:93]
	global_load_dword v50, v[52:53], off nt
	v_lshl_add_u64 v[52:53], v[52:53], 0, s[92:93]
	global_load_dword v51, v[52:53], off nt
	v_lshl_add_u64 v[54:55], v[52:53], 0, s[92:93]
	global_load_dword v52, v[54:55], off nt
	v_lshl_add_u64 v[54:55], v[54:55], 0, s[92:93]
	global_load_dword v53, v[54:55], off nt
	v_lshl_add_u64 v[56:57], v[54:55], 0, s[92:93]
	global_load_dword v54, v[56:57], off nt
	v_lshl_add_u64 v[56:57], v[56:57], 0, s[92:93]
	global_load_dword v55, v[56:57], off nt
	v_lshl_add_u64 v[58:59], v[56:57], 0, s[92:93]
	global_load_dword v56, v[58:59], off nt
	v_lshl_add_u64 v[58:59], v[58:59], 0, s[92:93]
	global_load_dword v57, v[58:59], off nt
	v_lshl_add_u64 v[60:61], v[58:59], 0, s[92:93]
	global_load_dword v58, v[60:61], off nt
	v_lshl_add_u64 v[60:61], v[60:61], 0, s[92:93]
	global_load_dword v59, v[60:61], off nt
	v_lshl_add_u64 v[62:63], v[60:61], 0, s[92:93]
	global_load_dword v60, v[62:63], off nt
	v_lshl_add_u64 v[62:63], v[62:63], 0, s[92:93]
	global_load_dword v61, v[62:63], off nt
	v_lshl_add_u64 v[64:65], v[62:63], 0, s[92:93]
	global_load_dword v62, v[64:65], off nt
	v_lshl_add_u64 v[64:65], v[64:65], 0, s[92:93]
	global_load_dword v63, v[64:65], off nt
	v_lshl_add_u64 v[66:67], v[64:65], 0, s[92:93]
	global_load_dword v64, v[66:67], off nt
	v_lshl_add_u64 v[66:67], v[66:67], 0, s[92:93]
	global_load_dword v65, v[66:67], off nt
	v_lshl_add_u64 v[68:69], v[66:67], 0, s[92:93]
	global_load_dword v66, v[68:69], off nt
	v_lshl_add_u64 v[68:69], v[68:69], 0, s[92:93]
	global_load_dword v67, v[68:69], off nt
	v_lshl_add_u64 v[70:71], v[68:69], 0, s[92:93]
	global_load_dword v68, v[70:71], off nt
	v_lshl_add_u64 v[70:71], v[70:71], 0, s[92:93]

.LBB0_585:
	s_cmp_lg_u32 s8, 2
	s_cselect_b32 s35, s34, 0x800
	s_cmp_eq_u32 s8, 1
	s_cselect_b32 s5, s16, s18
	s_cselect_b32 s6, s17, s19
	s_cmp_eq_u32 s8, 0
	s_cselect_b32 s8, s15, s6
	s_cselect_b32 s5, s14, s5
	s_lshl_b32 s6, s34, 11
	s_mul_hi_i32 s7, s11, s6
	s_mul_i32 s6, s11, s6
	s_lshl_b64 s[6:7], s[6:7], 2
	s_add_u32 s6, s5, s6
	v_or_b32_e32 v1, s10, v4
	s_addc_u32 s7, s8, s7
	v_mad_i64_i32 v[8:9], s[8:9], v1, s35, 0
	v_lshl_add_u64 v[8:9], v[8:9], 2, s[6:7]
	s_ashr_i32 s5, s4, 31
	v_lshl_add_u64 v[8:9], s[4:5], 2, v[8:9]
	v_lshlrev_b32_e32 v10, 2, v6
	v_mov_b32_e32 v11, v3
	v_lshl_add_u64 v[8:9], v[8:9], 0, v[10:11]
	s_lshl_b32 s92, s35, 2
	global_load_dword v1, v[8:9], off nt
	v_lshl_add_u64 v[8:9], v[8:9], 0, s[92:93]
	global_load_dword v5, v[8:9], off nt
	v_lshl_add_u64 v[8:9], v[8:9], 0, s[92:93]
	global_load_dword v7, v[8:9], off nt
	v_lshl_add_u64 v[10:11], v[8:9], 0, s[92:93]
	global_load_dword v8, v[10:11], off nt
	v_lshl_add_u64 v[10:11], v[10:11], 0, s[92:93]
	global_load_dword v9, v[10:11], off nt
	v_lshl_add_u64 v[12:13], v[10:11], 0, s[92:93]
	global_load_dword v10, v[12:13], off nt
	v_lshl_add_u64 v[12:13], v[12:13], 0, s[92:93]
	global_load_dword v11, v[12:13], off nt
	v_lshl_add_u64 v[14:15], v[12:13], 0, s[92:93]
	global_load_dword v12, v[14:15], off nt
	v_lshl_add_u64 v[14:15], v[14:15], 0, s[92:93]
	global_load_dword v13, v[14:15], off nt
	v_lshl_add_u64 v[16:17], v[14:15], 0, s[92:93]
	global_load_dword v14, v[16:17], off nt
	v_lshl_add_u64 v[16:17], v[16:17], 0, s[92:93]
	global_load_dword v15, v[16:17], off nt
	v_lshl_add_u64 v[18:19], v[16:17], 0, s[92:93]
	global_load_dword v16, v[18:19], off nt
	v_lshl_add_u64 v[18:19], v[18:19], 0, s[92:93]
	global_load_dword v17, v[18:19], off nt
	v_lshl_add_u64 v[20:21], v[18:19], 0, s[92:93]
	global_load_dword v18, v[20:21], off nt
	v_lshl_add_u64 v[20:21], v[20:21], 0, s[92:93]
	global_load_dword v19, v[20:21], off nt
	v_lshl_add_u64 v[22:23], v[20:21], 0, s[92:93]
	global_load_dword v20, v[22:23], off nt
	v_lshl_add_u64 v[22:23], v[22:23], 0, s[92:93]
	global_load_dword v21, v[22:23], off nt
	v_lshl_add_u64 v[24:25], v[22:23], 0, s[92:93]
	global_load_dword v22, v[24:25], off nt
	v_lshl_add_u64 v[24:25], v[24:25], 0, s[92:93]
	global_load_dword v23, v[24:25], off nt
	v_lshl_add_u64 v[26:27], v[24:25], 0, s[92:93]
	global_load_dword v24, v[26:27], off nt
	v_lshl_add_u64 v[26:27], v[26:27], 0, s[92:93]
	global_load_dword v25, v[26:27], off nt
	v_lshl_add_u64 v[28:29], v[26:27], 0, s[92:93]
	global_load_dword v26, v[28:29], off nt
	v_lshl_add_u64 v[28:29], v[28:29], 0, s[92:93]
	global_load_dword v27, v[28:29], off nt
	v_lshl_add_u64 v[30:31], v[28:29], 0, s[92:93]
	global_load_dword v28, v[30:31], off nt
	v_lshl_add_u64 v[30:31], v[30:31], 0, s[92:93]
	global_load_dword v29, v[30:31], off nt
	v_lshl_add_u64 v[32:33], v[30:31], 0, s[92:93]
	global_load_dword v30, v[32:33], off nt
	v_lshl_add_u64 v[32:33], v[32:33], 0, s[92:93]
	global_load_dword v31, v[32:33], off nt
	v_lshl_add_u64 v[34:35], v[32:33], 0, s[92:93]
	global_load_dword v32, v[34:35], off nt
	v_lshl_add_u64 v[34:35], v[34:35], 0, s[92:93]
	global_load_dword v33, v[34:35], off nt
	v_lshl_add_u64 v[70:71], v[34:35], 0, s[92:93]
	global_load_dword v34, v[70:71], off nt
	v_lshl_add_u64 v[70:71], v[70:71], 0, s[92:93]
	global_load_dword v35, v[70:71], off nt
	v_lshl_add_u64 v[70:71], v[70:71], 0, s[92:93]
	global_load_dword v36, v[70:71], off nt
	v_lshl_add_u64 v[70:71], v[70:71], 0, s[92:93]
